# v30 + ctx mini-GEMM loops over its 256 tiles with stride gridDim.x (robust to grid size; one tile per workgroup on 256 CUs)
# speedup vs baseline: 1.0184x; 1.0014x over previous
; #define PG8_LAS __attribute__((address_space(3)))
; #define SEAM(k) do { if (IN(k) && IN((k) + 1)) { if ((MK_TAIL_MASK >> (k)) & 1u) moe_pull(F, (k), 0); if ((k) == 9) moe_pull(F, -1, NQ_LATE); if ((k) == 15) moe_pull(F, -1, NQ); xcd_barrier(bar); { int t_ = threadIdx.x; asm volatile("" : "+v"(t_)); F.tid = t_; F.lane = t_ & 63; } } } while (0)
; template <class Epi, class Sched, bool ALIGN_EPI = false, bool SP2 = false, bool FP8 = false>
; __device__ __forceinline__ void gemm_phase(PG8_LAS unsigned char* lds, const Gemm g, const Sched& S, const Epi& E) {
;     int tid_ = threadIdx.x; asm volatile("" : "+v"(tid_));
;     const int tid = tid_, wid = __builtin_amdgcn_readfirstlane(tid >> 6), lane = tid & 63, wr = wid >> 2, wc = wid & 3, fr = lane & 15, fq = lane >> 4;
;     const int K = g.K, nt = g.KL / BK; const size_t kspl = (size_t)g.KL * 2;
;     unsigned voffA[2], voffB[2];
; #pragma unroll
;     for (int i = 0; i < 2; ++i) { int R, C; stage_rc(tid * 16 + i * 8192, R, C); const int Rb = Epi::PERM ? ((R & ~31) + perm32(R & 31)) : R;
;         voffA[i] = (unsigned)(R * K + C) * 2u; voffB[i] = (unsigned)(Rb * K + C) * 2u; }
;     const size_t kstep = (size_t)(BK * 2);
;     const size_t hstep = (size_t)HALF * K * 2;
;     const size_t tstep = 2 * hstep;
;     const unsigned ldsw = (unsigned)wid * 1024u;
;     const int aoff = lds_byte(wr * 64 + fr, fq * 8), boff = lds_byte(wc * 32 + fr, fq * 8);
; __global__ void __launch_bounds__(NWAVES * 64, 2) fwd_kernel(Args args) {
;     ...
;     if (IN(5)) { pg8::Gemm g{WSP(const pg8::bf16_t, WS_AO), WSP(const pg8::bf16_t, WS_WOUT0), MT, DM, DM, 0, DM, 0, 0}; pg8::StaticOrder S; S.init(MT, DM, F.G, (int)blockIdx.x);
;         pg8::EpiResH<false> E{F.in[0], F.in[2], WSP(pg8::bf16_t, WS_H), WSP(const float, WS_MOD0) + 2 * DM, 1.0f};
;         pg8::gemm_phase<pg8::EpiResH<false>, pg8::StaticOrder, true, true>(F.lds, g, S, E); } SEAM(5);
.LBB0_546:
	v_readlane_b32 s98, v250, 62
	s_nop 3
.Lmg5_tile:
	s_cmpk_gt_u32 s98, 0xff
	s_cbranch_scc1 .Lmg5_done
	v_and_b32_e32 v2, 15, v0
	v_bfe_u32 v3, v0, 4, 2
	v_lshrrev_b32_e32 v4, 6, v0
	v_lshrrev_b32_e32 v5, 1, v4
	v_and_b32_e32 v6, 1, v4
	s_lshr_b32 s99, s98, 5
	s_lshl_b32 s99, s99, 6
	s_and_b32 s100, s98, 31
	s_lshl_b32 s100, s100, 6
	v_lshl_add_u32 v7, v5, 4, v2
	v_add_u32_e32 v7, s99, v7
	v_lshrrev_b32_e32 v8, 4, v0
	v_lshlrev_b32_e32 v9, 4, v2
	v_add_u32_e32 v10, s99, v8
	v_mul_u32_u24_e32 v10, 0x1000, v10
	v_add_u32_e32 v10, v10, v9
	s_mov_b32 s101, 0x25c00000
	v_add_u32_e32 v10, s101, v10
	v_mov_b32_e32 v11, 0
	v_add_u32_e32 v12, 0x20000, v10
	v_mov_b32_e32 v13, 0
	v_add_u32_e32 v14, s100, v8
	v_mul_u32_u24_e32 v14, 0x1000, v14
	v_add_u32_e32 v14, v14, v9
	s_mov_b32 s101, 0x2600000
	v_add_u32_e32 v14, s101, v14
	v_mov_b32_e32 v15, 0
	v_add_u32_e32 v16, 0x20000, v14
	v_mov_b32_e32 v17, 0
	v_lshl_add_u64 v[10:11], s[88:89], 0, v[10:11]
	v_lshl_add_u64 v[12:13], s[88:89], 0, v[12:13]
	v_lshl_add_u64 v[14:15], s[88:89], 0, v[14:15]
	v_lshl_add_u64 v[16:17], s[88:89], 0, v[16:17]
	v_mul_u32_u24_e32 v18, 272, v8
	v_add_u32_e32 v18, v18, v9
	v_lshl_add_u32 v19, v5, 4, v2
	v_mul_u32_u24_e32 v19, 272, v19
	v_lshl_add_u32 v19, v3, 4, v19
	v_lshl_add_u32 v28, v6, 5, v2
	v_mul_u32_u24_e32 v28, 272, v28
	v_lshl_add_u32 v28, v3, 4, v28
	v_add_u32_e32 v28, 17408, v28
	v_mov_b32_e32 v112, 0x400
	v_mov_b32_e32 v113, 0
	v_lshl_add_u32 v116, v6, 5, s100
	v_lshl_add_u32 v116, v3, 2, v116
	v_lshlrev_b32_e32 v118, 2, v116
	v_lshl_add_u32 v128, v7, 13, v118
	v_mov_b32_e32 v129, 0
	v_readlane_b32 s100, v250, 12
	v_readlane_b32 s101, v250, 13
	s_nop 4
	v_lshl_add_u64 v[128:129], s[100:101], 0, v[128:129]
	s_mov_b32 s101, 0x11c000
	v_add_u32_e32 v130, s101, v118
	v_mov_b32_e32 v131, 0
	v_lshl_add_u64 v[130:131], s[88:89], 0, v[130:131]
	global_load_dwordx4 v[132:135], v[128:129], off
	global_load_dwordx4 v[136:139], v[128:129], off offset:64
	global_load_dwordx4 v[140:143], v[130:131], off
	global_load_dwordx4 v[144:147], v[130:131], off offset:64
	v_mov_b32_e32 v20, 0
	v_mov_b32_e32 v21, 0
	v_mov_b32_e32 v22, 0
	v_mov_b32_e32 v23, 0
	v_mov_b32_e32 v24, 0
	v_mov_b32_e32 v25, 0
	v_mov_b32_e32 v26, 0
	v_mov_b32_e32 v27, 0
	global_load_dwordx4 v[32:35], v[10:11], off offset:0
	global_load_dwordx4 v[36:39], v[12:13], off offset:0
	global_load_dwordx4 v[40:43], v[14:15], off offset:0
	global_load_dwordx4 v[44:47], v[16:17], off offset:0
	global_load_dwordx4 v[48:51], v[10:11], off offset:256
	global_load_dwordx4 v[52:55], v[12:13], off offset:256
	global_load_dwordx4 v[56:59], v[14:15], off offset:256
	global_load_dwordx4 v[60:63], v[16:17], off offset:256
	global_load_dwordx4 v[160:163], v[10:11], off offset:512
	global_load_dwordx4 v[164:167], v[12:13], off offset:512
	global_load_dwordx4 v[168:171], v[14:15], off offset:512
	global_load_dwordx4 v[172:175], v[16:17], off offset:512
	global_load_dwordx4 v[176:179], v[10:11], off offset:768
	global_load_dwordx4 v[180:183], v[12:13], off offset:768
	global_load_dwordx4 v[184:187], v[14:15], off offset:768
	global_load_dwordx4 v[188:191], v[16:17], off offset:768
	s_waitcnt vmcnt(12)
	ds_write_b128 v18, v[32:35] offset:0
	ds_write_b128 v18, v[36:39] offset:8704
	ds_write_b128 v18, v[40:43] offset:17408
	ds_write_b128 v18, v[44:47] offset:26112
	s_waitcnt lgkmcnt(0)
	s_barrier
	s_mov_b32 s101, 4
.Lmg5_kloop:
	global_load_dwordx4 v[32:35], v[10:11], off offset:1024
	global_load_dwordx4 v[36:39], v[12:13], off offset:1024
	global_load_dwordx4 v[40:43], v[14:15], off offset:1024
	global_load_dwordx4 v[44:47], v[16:17], off offset:1024
	s_waitcnt vmcnt(12)
	ds_write_b128 v18, v[48:51] offset:34816
	ds_write_b128 v18, v[52:55] offset:43520
	ds_write_b128 v18, v[56:59] offset:52224
	ds_write_b128 v18, v[60:63] offset:60928
	ds_read_b128 v[64:67], v19 offset:0
	ds_read_b128 v[68:71], v19 offset:64
	ds_read_b128 v[72:75], v19 offset:128
	ds_read_b128 v[76:79], v19 offset:192
	ds_read_b128 v[80:83], v28 offset:0
	ds_read_b128 v[84:87], v28 offset:64
	ds_read_b128 v[88:91], v28 offset:128
	ds_read_b128 v[92:95], v28 offset:192
	ds_read_b128 v[96:99], v28 offset:4352
	ds_read_b128 v[100:103], v28 offset:4416
	ds_read_b128 v[104:107], v28 offset:4480
	ds_read_b128 v[108:111], v28 offset:4544
	s_waitcnt lgkmcnt(0)
	v_mfma_f32_16x16x32_bf16 v[20:23], v[80:83], v[64:67], v[20:23]
	v_mfma_f32_16x16x32_bf16 v[24:27], v[96:99], v[64:67], v[24:27]
	v_mfma_f32_16x16x32_bf16 v[20:23], v[84:87], v[68:71], v[20:23]
	v_mfma_f32_16x16x32_bf16 v[24:27], v[100:103], v[68:71], v[24:27]
	v_mfma_f32_16x16x32_bf16 v[20:23], v[88:91], v[72:75], v[20:23]
	v_mfma_f32_16x16x32_bf16 v[24:27], v[104:107], v[72:75], v[24:27]
	v_mfma_f32_16x16x32_bf16 v[20:23], v[92:95], v[76:79], v[20:23]
	v_mfma_f32_16x16x32_bf16 v[24:27], v[108:111], v[76:79], v[24:27]
	s_waitcnt lgkmcnt(0)
	s_barrier
	global_load_dwordx4 v[48:51], v[10:11], off offset:1280
	global_load_dwordx4 v[52:55], v[12:13], off offset:1280
	global_load_dwordx4 v[56:59], v[14:15], off offset:1280
	global_load_dwordx4 v[60:63], v[16:17], off offset:1280
	s_waitcnt vmcnt(12)
	ds_write_b128 v18, v[160:163] offset:0
	ds_write_b128 v18, v[164:167] offset:8704
	ds_write_b128 v18, v[168:171] offset:17408
	ds_write_b128 v18, v[172:175] offset:26112
	ds_read_b128 v[64:67], v19 offset:34816
	ds_read_b128 v[68:71], v19 offset:34880
	ds_read_b128 v[72:75], v19 offset:34944
	ds_read_b128 v[76:79], v19 offset:35008
	ds_read_b128 v[80:83], v28 offset:34816
	ds_read_b128 v[84:87], v28 offset:34880
	ds_read_b128 v[88:91], v28 offset:34944
	ds_read_b128 v[92:95], v28 offset:35008
	ds_read_b128 v[96:99], v28 offset:39168
	ds_read_b128 v[100:103], v28 offset:39232
	ds_read_b128 v[104:107], v28 offset:39296
	ds_read_b128 v[108:111], v28 offset:39360
	s_waitcnt lgkmcnt(0)
	v_mfma_f32_16x16x32_bf16 v[20:23], v[80:83], v[64:67], v[20:23]
	v_mfma_f32_16x16x32_bf16 v[24:27], v[96:99], v[64:67], v[24:27]
	v_mfma_f32_16x16x32_bf16 v[20:23], v[84:87], v[68:71], v[20:23]
	v_mfma_f32_16x16x32_bf16 v[24:27], v[100:103], v[68:71], v[24:27]
	v_mfma_f32_16x16x32_bf16 v[20:23], v[88:91], v[72:75], v[20:23]
	v_mfma_f32_16x16x32_bf16 v[24:27], v[104:107], v[72:75], v[24:27]
	v_mfma_f32_16x16x32_bf16 v[20:23], v[92:95], v[76:79], v[20:23]
	v_mfma_f32_16x16x32_bf16 v[24:27], v[108:111], v[76:79], v[24:27]
	s_waitcnt lgkmcnt(0)
	s_barrier
; __device__ __forceinline__ unsigned cvt_pk_bf16(float lo, float hi) { unsigned r; asm volatile("v_cvt_pk_bf16_f32 %0, %1, %2" : "=v"(r) : "v"(lo), "v"(hi)); return r; }
;     __device__ __forceinline__ void operator()(const f32x4 (&acc)[2][2][4][2], const Unit& u, int wr, int wc, int fr, int fq) const {
;     ...
;                 const float* res = isc ? resC - (size_t)16384 * 2048 : resL;
;                 f32x4 bs[4][2][2];
; #pragma unroll
;                 for (int m = 0; m < 4; ++m)
; #pragma unroll
;                     for (int bj = 0; bj < 2; ++bj)
; #pragma unroll
;                         for (int n = 0; n < 2; ++n) bs[m][bj][n] = *(const f32x4*)(res + (size_t)(row0 + ai * HALF + m * 16) * 2048 + col0 + bj * HALF + n * 4);
; #pragma unroll
;                 for (int m = 0; m < 4; ++m)
; #pragma unroll
;                     for (int bj = 0; bj < 2; ++bj) { const f32x4 r0 = bs[m][bj][0] + gg[bj][0] * acc[ai][bj][m][0], r1 = bs[m][bj][1] + gg[bj][1] * acc[ai][bj][m][1];
;                         u32x4 w; w.x = cvt_pk_bf16(r0[0], r0[1]); w.y = cvt_pk_bf16(r0[2], r0[3]); w.z = cvt_pk_bf16(r1[0], r1[1]); w.w = cvt_pk_bf16(r1[2], r1[3]);
;                         *(u32x4*)(H + (size_t)(row0 + ai * HALF + m * 16) * 2048 + col0 + bj * HALF) = w; }
; __device__ __forceinline__ void xcd_barrier(const XcdBarrier& b) {
;     asm volatile("s_waitcnt vmcnt(0)" ::: "memory");
;     __syncthreads();
;     if (threadIdx.x == 0) {
;         unsigned* bar = b.bar;
;         __builtin_amdgcn_s_waitcnt(0);
;         unsigned nloc = b.st[0], nx = b.st[1];
;         if (nloc == 0u) { xcd_barrier_complete(bar, b.x, b.total, nloc, nx); b.st[0] = nloc; b.st[1] = nx; }
	global_load_dwordx4 v[160:163], v[10:11], off offset:1536
	global_load_dwordx4 v[164:167], v[12:13], off offset:1536
	global_load_dwordx4 v[168:171], v[14:15], off offset:1536
	global_load_dwordx4 v[172:175], v[16:17], off offset:1536
	s_waitcnt vmcnt(12)
	ds_write_b128 v18, v[176:179] offset:34816
	ds_write_b128 v18, v[180:183] offset:43520
	ds_write_b128 v18, v[184:187] offset:52224
	ds_write_b128 v18, v[188:191] offset:60928
	ds_read_b128 v[64:67], v19 offset:0
	ds_read_b128 v[68:71], v19 offset:64
	ds_read_b128 v[72:75], v19 offset:128
	ds_read_b128 v[76:79], v19 offset:192
	ds_read_b128 v[80:83], v28 offset:0
	ds_read_b128 v[84:87], v28 offset:64
	ds_read_b128 v[88:91], v28 offset:128
	ds_read_b128 v[92:95], v28 offset:192
	ds_read_b128 v[96:99], v28 offset:4352
	ds_read_b128 v[100:103], v28 offset:4416
	ds_read_b128 v[104:107], v28 offset:4480
	ds_read_b128 v[108:111], v28 offset:4544
	s_waitcnt lgkmcnt(0)
	v_mfma_f32_16x16x32_bf16 v[20:23], v[80:83], v[64:67], v[20:23]
	v_mfma_f32_16x16x32_bf16 v[24:27], v[96:99], v[64:67], v[24:27]
	v_mfma_f32_16x16x32_bf16 v[20:23], v[84:87], v[68:71], v[20:23]
	v_mfma_f32_16x16x32_bf16 v[24:27], v[100:103], v[68:71], v[24:27]
	v_mfma_f32_16x16x32_bf16 v[20:23], v[88:91], v[72:75], v[20:23]
	v_mfma_f32_16x16x32_bf16 v[24:27], v[104:107], v[72:75], v[24:27]
	v_mfma_f32_16x16x32_bf16 v[20:23], v[92:95], v[76:79], v[20:23]
	v_mfma_f32_16x16x32_bf16 v[24:27], v[108:111], v[76:79], v[24:27]
	s_waitcnt lgkmcnt(0)
	s_barrier
	global_load_dwordx4 v[176:179], v[10:11], off offset:1792
	global_load_dwordx4 v[180:183], v[12:13], off offset:1792
	global_load_dwordx4 v[184:187], v[14:15], off offset:1792
	global_load_dwordx4 v[188:191], v[16:17], off offset:1792
	s_waitcnt vmcnt(12)
	ds_write_b128 v18, v[32:35] offset:0
	ds_write_b128 v18, v[36:39] offset:8704
	ds_write_b128 v18, v[40:43] offset:17408
	ds_write_b128 v18, v[44:47] offset:26112
	ds_read_b128 v[64:67], v19 offset:34816
	ds_read_b128 v[68:71], v19 offset:34880
	ds_read_b128 v[72:75], v19 offset:34944
	ds_read_b128 v[76:79], v19 offset:35008
	ds_read_b128 v[80:83], v28 offset:34816
	ds_read_b128 v[84:87], v28 offset:34880
	ds_read_b128 v[88:91], v28 offset:34944
	ds_read_b128 v[92:95], v28 offset:35008
	ds_read_b128 v[96:99], v28 offset:39168
	ds_read_b128 v[100:103], v28 offset:39232
	ds_read_b128 v[104:107], v28 offset:39296
	ds_read_b128 v[108:111], v28 offset:39360
	s_waitcnt lgkmcnt(0)
	v_mfma_f32_16x16x32_bf16 v[20:23], v[80:83], v[64:67], v[20:23]
	v_mfma_f32_16x16x32_bf16 v[24:27], v[96:99], v[64:67], v[24:27]
	v_mfma_f32_16x16x32_bf16 v[20:23], v[84:87], v[68:71], v[20:23]
	v_mfma_f32_16x16x32_bf16 v[24:27], v[100:103], v[68:71], v[24:27]
	v_mfma_f32_16x16x32_bf16 v[20:23], v[88:91], v[72:75], v[20:23]
	v_mfma_f32_16x16x32_bf16 v[24:27], v[104:107], v[72:75], v[24:27]
	v_mfma_f32_16x16x32_bf16 v[20:23], v[92:95], v[76:79], v[20:23]
	v_mfma_f32_16x16x32_bf16 v[24:27], v[108:111], v[76:79], v[24:27]
	v_lshl_add_u64 v[10:11], v[10:11], 0, v[112:113]
	v_lshl_add_u64 v[12:13], v[12:13], 0, v[112:113]
	v_lshl_add_u64 v[14:15], v[14:15], 0, v[112:113]
	v_lshl_add_u64 v[16:17], v[16:17], 0, v[112:113]
	s_waitcnt lgkmcnt(0)
	s_barrier
	s_sub_u32 s101, s101, 1
	s_cmp_lg_u32 s101, 0
	s_cbranch_scc1 .Lmg5_kloop
	s_nop 7
	s_nop 7
	v_lshlrev_b32_e32 v116, 1, v116
	v_lshl_add_u32 v116, v7, 12, v116
	s_mov_b32 s101, 0x51800000
	v_add_u32_e32 v116, s101, v116
	v_mov_b32_e32 v117, 0
	v_lshl_add_u64 v[116:117], s[88:89], 0, v[116:117]
	v_fma_f32 v20, v140, v20, v132
	v_fma_f32 v21, v141, v21, v133
	v_fma_f32 v22, v142, v22, v134
	v_fma_f32 v23, v143, v23, v135
	v_fma_f32 v24, v144, v24, v136
	v_fma_f32 v25, v145, v25, v137
	v_fma_f32 v26, v146, v26, v138
	v_fma_f32 v27, v147, v27, v139
	v_cvt_pk_bf16_f32 v28, v20, v21
	v_cvt_pk_bf16_f32 v29, v22, v23
	v_cvt_pk_bf16_f32 v30, v24, v25
	v_cvt_pk_bf16_f32 v31, v26, v27
	global_store_dwordx2 v[116:117], v[28:29], off
	global_store_dwordx2 v[116:117], v[30:31], off offset:32
	s_add_u32 s98, s98, s93
	s_branch .Lmg5_tile
.Lmg5_done:
	s_cmp_gt_i32 s91, 6
	s_cselect_b64 s[0:1], -1, 0
	s_and_b64 s[2:3], s[2:3], s[0:1]
	s_andn2_b64 vcc, exec, s[2:3]
	s_cbranch_vccnz .LBB0_600
	s_waitcnt vmcnt(0)
	s_waitcnt vmcnt(0) lgkmcnt(0)
	s_barrier
	s_mov_b64 s[2:3], exec
	v_readlane_b32 s4, v250, 59
	v_readlane_b32 s5, v250, 60
	s_and_b64 s[4:5], s[2:3], s[4:5]
	s_mov_b64 exec, s[4:5]
	s_cbranch_execz .LBB0_599
	s_add_i32 s4, 0, 0x25020
	v_mov_b32_e32 v1, s4
	s_waitcnt vmcnt(0) expcnt(0) lgkmcnt(0)
	ds_read_b32 v3, v1
	s_add_i32 s4, 0, 0x25024
	v_mov_b32_e32 v1, s4
	ds_read_b32 v1, v1
	s_waitcnt lgkmcnt(1)
	v_cmp_ne_u32_e32 vcc, 0, v3
	s_cbranch_vccnz .LBB0_563
	s_add_u32 s4, s88, 0x4200
	s_addc_u32 s5, s89, 0
	s_add_u32 s6, s88, 0x4400
	s_addc_u32 s7, s89, 0
	s_add_u32 s8, s88, 0x4500
	s_addc_u32 s9, s89, 0
	s_add_u32 s10, s88, 0x4600
	s_addc_u32 s11, s89, 0
	s_add_u32 s12, s88, 0x4700
	s_addc_u32 s13, s89, 0
	s_add_u32 s14, s88, 0x4800
	s_addc_u32 s15, s89, 0
	s_add_u32 s16, s88, 0x4900
	s_addc_u32 s17, s89, 0
	s_add_u32 s18, s88, 0x4a00
	s_addc_u32 s19, s89, 0
	s_add_u32 s20, s88, 0x4b00
	s_addc_u32 s21, s89, 0
	s_add_u32 s22, s88, 0x4c00
	s_addc_u32 s23, s89, 0
	s_add_u32 s24, s88, 0x4d00
	s_addc_u32 s25, s89, 0
	s_add_u32 s26, s88, 0x4e00
	s_addc_u32 s27, s89, 0
	s_add_u32 s28, s88, 0x4f00
	s_addc_u32 s29, s89, 0
	s_add_u32 s30, s88, 0x5000
	s_addc_u32 s31, s89, 0
	s_add_u32 s34, s88, 0x5100
	s_addc_u32 s35, s89, 0
	s_add_u32 s36, s88, 0x5200
	s_addc_u32 s37, s89, 0
	s_add_u32 s38, s88, 0x5300
	s_addc_u32 s39, s89, 0
	s_mov_b32 s33, 1
	v_mov_b32_e32 v17, 0
	s_branch .LBB0_551

; #define PG8_LAS __attribute__((address_space(3)))
; #define SEAM(k) do { if (IN(k) && IN((k) + 1)) { if ((MK_TAIL_MASK >> (k)) & 1u) moe_pull(F, (k), 0); if ((k) == 9) moe_pull(F, -1, NQ_LATE); if ((k) == 15) moe_pull(F, -1, NQ); xcd_barrier(bar); { int t_ = threadIdx.x; asm volatile("" : "+v"(t_)); F.tid = t_; F.lane = t_ & 63; } } } while (0)
; template <class Epi, class Sched, bool ALIGN_EPI = false, bool SP2 = false, bool FP8 = false>
; __device__ __forceinline__ void gemm_phase(PG8_LAS unsigned char* lds, const Gemm g, const Sched& S, const Epi& E) {
;     int tid_ = threadIdx.x; asm volatile("" : "+v"(tid_));
;     const int tid = tid_, wid = __builtin_amdgcn_readfirstlane(tid >> 6), lane = tid & 63, wr = wid >> 2, wc = wid & 3, fr = lane & 15, fq = lane >> 4;
;     const int K = g.K, nt = g.KL / BK; const size_t kspl = (size_t)g.KL * 2;
;     unsigned voffA[2], voffB[2];
; #pragma unroll
;     for (int i = 0; i < 2; ++i) { int R, C; stage_rc(tid * 16 + i * 8192, R, C); const int Rb = Epi::PERM ? ((R & ~31) + perm32(R & 31)) : R;
;         voffA[i] = (unsigned)(R * K + C) * 2u; voffB[i] = (unsigned)(Rb * K + C) * 2u; }
;     const size_t kstep = (size_t)(BK * 2);
;     const size_t hstep = (size_t)HALF * K * 2;
;     const size_t tstep = 2 * hstep;
;     const unsigned ldsw = (unsigned)wid * 1024u;
;     const int aoff = lds_byte(wr * 64 + fr, fq * 8), boff = lds_byte(wc * 32 + fr, fq * 8);
; __global__ void __launch_bounds__(NWAVES * 64, 2) fwd_kernel(Args args) {
;     ...
;     if (IN(10)) { pg8::Gemm g{XN, WSP(const pg8::bf16_t, WS_WIN1), MT, 2 * DM, DM, 0, DM, 0, 0}; pg8::StaticOrder S; S.init(MT, 2 * DM, F.G, (int)blockIdx.x);
;         pg8::EpiBf16 E{WSP(pg8::bf16_t, WS_Z), 2 * DM, 8, 0, 1.0f};
;         pg8::gemm_phase<pg8::EpiBf16, pg8::StaticOrder, true, true>(F.lds, g, S, E); } SEAM(10);
.Lmg10_tile:
	s_cmpk_gt_u32 s98, 0xff
	s_cbranch_scc1 .Lmg10_done
	v_and_b32_e32 v2, 15, v0
	v_bfe_u32 v3, v0, 4, 2
	v_lshrrev_b32_e32 v4, 6, v0
	v_lshrrev_b32_e32 v5, 1, v4
	v_and_b32_e32 v6, 1, v4
	s_lshr_b32 s99, s98, 5
	s_lshl_b32 s99, s99, 6
	s_and_b32 s100, s98, 31
	s_lshl_b32 s100, s100, 6
	v_lshl_add_u32 v7, v5, 4, v2
	v_add_u32_e32 v7, s99, v7
	v_lshrrev_b32_e32 v8, 4, v0
	v_lshlrev_b32_e32 v9, 4, v2
	v_add_u32_e32 v10, s99, v8
	v_mul_u32_u24_e32 v10, 0x1000, v10
	v_add_u32_e32 v10, v10, v9
	s_mov_b32 s101, 0x21a00000
	v_add_u32_e32 v10, s101, v10
	v_mov_b32_e32 v11, 0
	v_add_u32_e32 v12, 0x20000, v10
	v_mov_b32_e32 v13, 0
	v_add_u32_e32 v14, s100, v8
	v_mul_u32_u24_e32 v14, 0x1000, v14
	v_add_u32_e32 v14, v14, v9
	s_mov_b32 s101, 0x7800000
	v_add_u32_e32 v14, s101, v14
	v_mov_b32_e32 v15, 0
	v_add_u32_e32 v16, 0x20000, v14
	v_mov_b32_e32 v17, 0
	v_lshl_add_u64 v[10:11], s[88:89], 0, v[10:11]
	v_lshl_add_u64 v[12:13], s[88:89], 0, v[12:13]
	v_lshl_add_u64 v[14:15], s[88:89], 0, v[14:15]
	v_lshl_add_u64 v[16:17], s[88:89], 0, v[16:17]
	v_mul_u32_u24_e32 v18, 272, v8
	v_add_u32_e32 v18, v18, v9
	v_lshl_add_u32 v19, v5, 4, v2
	v_mul_u32_u24_e32 v19, 272, v19
	v_lshl_add_u32 v19, v3, 4, v19
	v_lshl_add_u32 v28, v6, 5, v2
	v_mul_u32_u24_e32 v28, 272, v28
	v_lshl_add_u32 v28, v3, 4, v28
	v_add_u32_e32 v28, 17408, v28
	v_mov_b32_e32 v112, 0x400
	v_mov_b32_e32 v113, 0
	v_mov_b32_e32 v20, 0
	v_mov_b32_e32 v21, 0
	v_mov_b32_e32 v22, 0
	v_mov_b32_e32 v23, 0
	v_mov_b32_e32 v24, 0
	v_mov_b32_e32 v25, 0
	v_mov_b32_e32 v26, 0
	v_mov_b32_e32 v27, 0
	global_load_dwordx4 v[32:35], v[10:11], off offset:0
	global_load_dwordx4 v[36:39], v[12:13], off offset:0
	global_load_dwordx4 v[40:43], v[14:15], off offset:0
	global_load_dwordx4 v[44:47], v[16:17], off offset:0
	global_load_dwordx4 v[48:51], v[10:11], off offset:256
	global_load_dwordx4 v[52:55], v[12:13], off offset:256
	global_load_dwordx4 v[56:59], v[14:15], off offset:256
	global_load_dwordx4 v[60:63], v[16:17], off offset:256
	global_load_dwordx4 v[160:163], v[10:11], off offset:512
	global_load_dwordx4 v[164:167], v[12:13], off offset:512
	global_load_dwordx4 v[168:171], v[14:15], off offset:512
	global_load_dwordx4 v[172:175], v[16:17], off offset:512
	global_load_dwordx4 v[176:179], v[10:11], off offset:768
	global_load_dwordx4 v[180:183], v[12:13], off offset:768
	global_load_dwordx4 v[184:187], v[14:15], off offset:768
	global_load_dwordx4 v[188:191], v[16:17], off offset:768
	s_waitcnt vmcnt(12)
	ds_write_b128 v18, v[32:35] offset:0
	ds_write_b128 v18, v[36:39] offset:8704
	ds_write_b128 v18, v[40:43] offset:17408
	ds_write_b128 v18, v[44:47] offset:26112
	s_waitcnt lgkmcnt(0)
	s_barrier
	s_mov_b32 s101, 4
.Lmg10_kloop:
	global_load_dwordx4 v[32:35], v[10:11], off offset:1024
	global_load_dwordx4 v[36:39], v[12:13], off offset:1024
	global_load_dwordx4 v[40:43], v[14:15], off offset:1024
	global_load_dwordx4 v[44:47], v[16:17], off offset:1024
	s_waitcnt vmcnt(12)
	ds_write_b128 v18, v[48:51] offset:34816
	ds_write_b128 v18, v[52:55] offset:43520
	ds_write_b128 v18, v[56:59] offset:52224
	ds_write_b128 v18, v[60:63] offset:60928
	ds_read_b128 v[64:67], v19 offset:0
	ds_read_b128 v[68:71], v19 offset:64
	ds_read_b128 v[72:75], v19 offset:128
	ds_read_b128 v[76:79], v19 offset:192
	ds_read_b128 v[80:83], v28 offset:0
	ds_read_b128 v[84:87], v28 offset:64
	ds_read_b128 v[88:91], v28 offset:128
	ds_read_b128 v[92:95], v28 offset:192
	ds_read_b128 v[96:99], v28 offset:4352
	ds_read_b128 v[100:103], v28 offset:4416
	ds_read_b128 v[104:107], v28 offset:4480
	ds_read_b128 v[108:111], v28 offset:4544
	s_waitcnt lgkmcnt(0)
	v_mfma_f32_16x16x32_bf16 v[20:23], v[80:83], v[64:67], v[20:23]
	v_mfma_f32_16x16x32_bf16 v[24:27], v[96:99], v[64:67], v[24:27]
	v_mfma_f32_16x16x32_bf16 v[20:23], v[84:87], v[68:71], v[20:23]
	v_mfma_f32_16x16x32_bf16 v[24:27], v[100:103], v[68:71], v[24:27]
	v_mfma_f32_16x16x32_bf16 v[20:23], v[88:91], v[72:75], v[20:23]
	v_mfma_f32_16x16x32_bf16 v[24:27], v[104:107], v[72:75], v[24:27]
	v_mfma_f32_16x16x32_bf16 v[20:23], v[92:95], v[76:79], v[20:23]
	v_mfma_f32_16x16x32_bf16 v[24:27], v[108:111], v[76:79], v[24:27]
	s_waitcnt lgkmcnt(0)
	s_barrier
	global_load_dwordx4 v[48:51], v[10:11], off offset:1280
	global_load_dwordx4 v[52:55], v[12:13], off offset:1280
	global_load_dwordx4 v[56:59], v[14:15], off offset:1280
	global_load_dwordx4 v[60:63], v[16:17], off offset:1280
	s_waitcnt vmcnt(12)
	ds_write_b128 v18, v[160:163] offset:0
	ds_write_b128 v18, v[164:167] offset:8704
	ds_write_b128 v18, v[168:171] offset:17408
	ds_write_b128 v18, v[172:175] offset:26112
	ds_read_b128 v[64:67], v19 offset:34816
	ds_read_b128 v[68:71], v19 offset:34880
	ds_read_b128 v[72:75], v19 offset:34944
	ds_read_b128 v[76:79], v19 offset:35008
	ds_read_b128 v[80:83], v28 offset:34816
	ds_read_b128 v[84:87], v28 offset:34880
	ds_read_b128 v[88:91], v28 offset:34944
	ds_read_b128 v[92:95], v28 offset:35008
	ds_read_b128 v[96:99], v28 offset:39168
	ds_read_b128 v[100:103], v28 offset:39232
	ds_read_b128 v[104:107], v28 offset:39296
	ds_read_b128 v[108:111], v28 offset:39360
	s_waitcnt lgkmcnt(0)
	v_mfma_f32_16x16x32_bf16 v[20:23], v[80:83], v[64:67], v[20:23]
	v_mfma_f32_16x16x32_bf16 v[24:27], v[96:99], v[64:67], v[24:27]
	v_mfma_f32_16x16x32_bf16 v[20:23], v[84:87], v[68:71], v[20:23]
	v_mfma_f32_16x16x32_bf16 v[24:27], v[100:103], v[68:71], v[24:27]
	v_mfma_f32_16x16x32_bf16 v[20:23], v[88:91], v[72:75], v[20:23]
	v_mfma_f32_16x16x32_bf16 v[24:27], v[104:107], v[72:75], v[24:27]
	v_mfma_f32_16x16x32_bf16 v[20:23], v[92:95], v[76:79], v[20:23]
	v_mfma_f32_16x16x32_bf16 v[24:27], v[108:111], v[76:79], v[24:27]
	s_waitcnt lgkmcnt(0)
	s_barrier
; #define SEAM(k) do { if (IN(k) && IN((k) + 1)) { if ((MK_TAIL_MASK >> (k)) & 1u) moe_pull(F, (k), 0); if ((k) == 9) moe_pull(F, -1, NQ_LATE); if ((k) == 15) moe_pull(F, -1, NQ); xcd_barrier(bar); { int t_ = threadIdx.x; asm volatile("" : "+v"(t_)); F.tid = t_; F.lane = t_ & 63; } } } while (0)
; __device__ __forceinline__ void xcd_barrier(const XcdBarrier& b) {
;     asm volatile("s_waitcnt vmcnt(0)" ::: "memory");
;     __syncthreads();
;     if (threadIdx.x == 0) {
;         unsigned* bar = b.bar;
;         __builtin_amdgcn_s_waitcnt(0);
;         unsigned nloc = b.st[0], nx = b.st[1];
;         if (nloc == 0u) { xcd_barrier_complete(bar, b.x, b.total, nloc, nx); b.st[0] = nloc; b.st[1] = nx; }
; __global__ void __launch_bounds__(NWAVES * 64, 2) fwd_kernel(Args args) {
;     ...
;     if (IN(10)) { pg8::Gemm g{XN, WSP(const pg8::bf16_t, WS_WIN1), MT, 2 * DM, DM, 0, DM, 0, 0}; pg8::StaticOrder S; S.init(MT, 2 * DM, F.G, (int)blockIdx.x);
;         pg8::EpiBf16 E{WSP(pg8::bf16_t, WS_Z), 2 * DM, 8, 0, 1.0f};
;         pg8::gemm_phase<pg8::EpiBf16, pg8::StaticOrder, true, true>(F.lds, g, S, E); } SEAM(10);
	global_load_dwordx4 v[160:163], v[10:11], off offset:1536
	global_load_dwordx4 v[164:167], v[12:13], off offset:1536
	global_load_dwordx4 v[168:171], v[14:15], off offset:1536
	global_load_dwordx4 v[172:175], v[16:17], off offset:1536
	s_waitcnt vmcnt(12)
	ds_write_b128 v18, v[176:179] offset:34816
	ds_write_b128 v18, v[180:183] offset:43520
	ds_write_b128 v18, v[184:187] offset:52224
	ds_write_b128 v18, v[188:191] offset:60928
	ds_read_b128 v[64:67], v19 offset:0
	ds_read_b128 v[68:71], v19 offset:64
	ds_read_b128 v[72:75], v19 offset:128
	ds_read_b128 v[76:79], v19 offset:192
	ds_read_b128 v[80:83], v28 offset:0
	ds_read_b128 v[84:87], v28 offset:64
	ds_read_b128 v[88:91], v28 offset:128
	ds_read_b128 v[92:95], v28 offset:192
	ds_read_b128 v[96:99], v28 offset:4352
	ds_read_b128 v[100:103], v28 offset:4416
	ds_read_b128 v[104:107], v28 offset:4480
	ds_read_b128 v[108:111], v28 offset:4544
	s_waitcnt lgkmcnt(0)
	v_mfma_f32_16x16x32_bf16 v[20:23], v[80:83], v[64:67], v[20:23]
	v_mfma_f32_16x16x32_bf16 v[24:27], v[96:99], v[64:67], v[24:27]
	v_mfma_f32_16x16x32_bf16 v[20:23], v[84:87], v[68:71], v[20:23]
	v_mfma_f32_16x16x32_bf16 v[24:27], v[100:103], v[68:71], v[24:27]
	v_mfma_f32_16x16x32_bf16 v[20:23], v[88:91], v[72:75], v[20:23]
	v_mfma_f32_16x16x32_bf16 v[24:27], v[104:107], v[72:75], v[24:27]
	v_mfma_f32_16x16x32_bf16 v[20:23], v[92:95], v[76:79], v[20:23]
	v_mfma_f32_16x16x32_bf16 v[24:27], v[108:111], v[76:79], v[24:27]
	s_waitcnt lgkmcnt(0)
	s_barrier
	global_load_dwordx4 v[176:179], v[10:11], off offset:1792
	global_load_dwordx4 v[180:183], v[12:13], off offset:1792
	global_load_dwordx4 v[184:187], v[14:15], off offset:1792
	global_load_dwordx4 v[188:191], v[16:17], off offset:1792
	s_waitcnt vmcnt(12)
	ds_write_b128 v18, v[32:35] offset:0
	ds_write_b128 v18, v[36:39] offset:8704
	ds_write_b128 v18, v[40:43] offset:17408
	ds_write_b128 v18, v[44:47] offset:26112
	ds_read_b128 v[64:67], v19 offset:34816
	ds_read_b128 v[68:71], v19 offset:34880
	ds_read_b128 v[72:75], v19 offset:34944
	ds_read_b128 v[76:79], v19 offset:35008
	ds_read_b128 v[80:83], v28 offset:34816
	ds_read_b128 v[84:87], v28 offset:34880
	ds_read_b128 v[88:91], v28 offset:34944
	ds_read_b128 v[92:95], v28 offset:35008
	ds_read_b128 v[96:99], v28 offset:39168
	ds_read_b128 v[100:103], v28 offset:39232
	ds_read_b128 v[104:107], v28 offset:39296
	ds_read_b128 v[108:111], v28 offset:39360
	s_waitcnt lgkmcnt(0)
	v_mfma_f32_16x16x32_bf16 v[20:23], v[80:83], v[64:67], v[20:23]
	v_mfma_f32_16x16x32_bf16 v[24:27], v[96:99], v[64:67], v[24:27]
	v_mfma_f32_16x16x32_bf16 v[20:23], v[84:87], v[68:71], v[20:23]
	v_mfma_f32_16x16x32_bf16 v[24:27], v[100:103], v[68:71], v[24:27]
	v_mfma_f32_16x16x32_bf16 v[20:23], v[88:91], v[72:75], v[20:23]
	v_mfma_f32_16x16x32_bf16 v[24:27], v[104:107], v[72:75], v[24:27]
	v_mfma_f32_16x16x32_bf16 v[20:23], v[92:95], v[76:79], v[20:23]
	v_mfma_f32_16x16x32_bf16 v[24:27], v[108:111], v[76:79], v[24:27]
	v_lshl_add_u64 v[10:11], v[10:11], 0, v[112:113]
	v_lshl_add_u64 v[12:13], v[12:13], 0, v[112:113]
	v_lshl_add_u64 v[14:15], v[14:15], 0, v[112:113]
	v_lshl_add_u64 v[16:17], v[16:17], 0, v[112:113]
	s_waitcnt lgkmcnt(0)
	s_barrier
	s_sub_u32 s101, s101, 1
	s_cmp_lg_u32 s101, 0
	s_cbranch_scc1 .Lmg10_kloop
	s_nop 7
	s_nop 7
	v_lshl_add_u32 v116, v6, 5, s100
	v_lshl_add_u32 v116, v3, 2, v116
	v_lshlrev_b32_e32 v116, 1, v116
	v_lshl_add_u32 v116, v7, 13, v116
	s_mov_b32 s101, 0x2e701000
	v_add_u32_e32 v116, s101, v116
	v_mov_b32_e32 v117, 0
	v_lshl_add_u64 v[116:117], s[88:89], 0, v[116:117]
	v_cvt_pk_bf16_f32 v28, v20, v21
	v_cvt_pk_bf16_f32 v29, v22, v23
	v_cvt_pk_bf16_f32 v30, v24, v25
	v_cvt_pk_bf16_f32 v31, v26, v27
	global_store_dwordx2 v[116:117], v[28:29], off
	global_store_dwordx2 v[116:117], v[30:31], off offset:32
	s_add_u32 s98, s98, s93
	s_branch .Lmg10_tile
.Lmg10_done:
	s_cmp_gt_i32 s91, 11
	s_cselect_b64 s[0:1], -1, 0
	s_and_b64 s[2:3], s[4:5], s[0:1]
	s_andn2_b64 vcc, exec, s[2:3]
	s_cbranch_vccnz .LBB0_1351
	s_waitcnt vmcnt(0)
	s_waitcnt vmcnt(0) lgkmcnt(0)
	s_barrier
	s_mov_b64 s[2:3], exec
	v_readlane_b32 s4, v250, 59
	v_readlane_b32 s5, v250, 60
	s_and_b64 s[4:5], s[2:3], s[4:5]
	s_mov_b64 exec, s[4:5]
	s_cbranch_execz .LBB0_1350
	s_add_i32 s4, 0, 0x25020
	v_mov_b32_e32 v1, s4
	s_waitcnt vmcnt(0) expcnt(0) lgkmcnt(0)
	ds_read_b32 v3, v1
	s_add_i32 s4, 0, 0x25024
	v_mov_b32_e32 v1, s4
	ds_read_b32 v1, v1
	s_waitcnt lgkmcnt(1)
	v_cmp_ne_u32_e32 vcc, 0, v3
	s_cbranch_vccnz .LBB0_1314
	s_add_u32 s4, s88, 0x4200
	s_addc_u32 s5, s89, 0
	s_add_u32 s6, s88, 0x4400
	s_addc_u32 s7, s89, 0
	s_add_u32 s8, s88, 0x4500
	s_addc_u32 s9, s89, 0
	s_add_u32 s10, s88, 0x4600
	s_addc_u32 s11, s89, 0
	s_add_u32 s12, s88, 0x4700
	s_addc_u32 s13, s89, 0
	s_add_u32 s14, s88, 0x4800
	s_addc_u32 s15, s89, 0
	s_add_u32 s16, s88, 0x4900
	s_addc_u32 s17, s89, 0
	s_add_u32 s18, s88, 0x4a00
	s_addc_u32 s19, s89, 0
	s_add_u32 s20, s88, 0x4b00
	s_addc_u32 s21, s89, 0
	s_add_u32 s22, s88, 0x4c00
	s_addc_u32 s23, s89, 0
	s_add_u32 s24, s88, 0x4d00
	s_addc_u32 s25, s89, 0
	s_add_u32 s26, s88, 0x4e00
	s_addc_u32 s27, s89, 0
	s_add_u32 s28, s88, 0x4f00
	s_addc_u32 s29, s89, 0
	s_add_u32 s30, s88, 0x5000
	s_addc_u32 s31, s89, 0
	s_add_u32 s34, s88, 0x5100
	s_addc_u32 s35, s89, 0
	s_add_u32 s36, s88, 0x5200
	s_addc_u32 s37, s89, 0
	s_add_u32 s38, s88, 0x5300
	s_addc_u32 s39, s89, 0
	s_mov_b32 s33, 1
	v_mov_b32_e32 v17, 0
	s_branch .LBB0_1302
